# v13b: v8 + scan state waves at s_setprio 1 only during the triangular solve (0 while stepping chunks)
# baseline (speedup 1.0000x reference)
.LBB0_1726:
	s_setprio 1
	s_add_i32 s0, s71, -1
	s_lshl_b32 s1, s83, 2
	s_add_i32 s1, s1, 0xc400
	v_cmp_eq_u32_e32 vcc, 0, v0
	v_mov_b32_e32 v18, s1
	v_mov_b32_e32 v19, s0
	s_and_saveexec_b64 s[0:1], vcc
	s_cbranch_execz .Lx14_pub_skip
	global_store_dword v18, v19, s[54:55] sc1

.LBB0_1728:
	s_or_b64 exec, exec, s[68:69]
	s_waitcnt lgkmcnt(0)
	s_and_saveexec_b64 s[68:69], s[4:5]
	s_add_i32 s0, s71, 1
	v_mov_b32_e32 v18, s61
	v_mov_b32_e32 v19, s0
	ds_write_b32 v18, v19
	s_setprio 0
	s_or_b64 exec, exec, s[68:69]
	s_lshl_b32 s68, s71, 2
	s_mov_b32 s69, 0
	s_branch .LBB0_1732
